# v028 + LRU loop: counted top-of-unit wait (no store drain) + scan passes with registers reused across both passes + packed gelu output stage
# speedup vs baseline: 1.0072x; 1.0072x over previous
; __device__ __forceinline__ unsigned pk2(float lo, float hi) { const f32x2c_t v = {lo, hi}; const bf16x2c_t b = __builtin_convertvector(v, bf16x2c_t); return __builtin_bit_cast(unsigned, b); }
; __device__ __forceinline__ float bflo(unsigned w) { return __uint_as_float(w << 16); }
; __device__ __forceinline__ float bfhi(unsigned w) { return __uint_as_float(w & 0xffff0000u); }
; __device__ __forceinline__ float gelu_tanh(float x) { const float y = 0.7978845608028654f * (x + 0.044715f * x * x * x); return x * __builtin_amdgcn_rcpf(1.0f + fexp_(-2.0f * y)); }
; template <int MODE> ...
;     ...
;             float acum = 1.f;
; #pragma unroll
;             for (int s2 = 0; s2 < 3; ++s2) if (s2 < seg) acum *= SEG[s2 * 128 + sj];
;             float hcur = hin;
; #pragma unroll
;             for (int q = 0; q < 16; ++q) { const int o = (seg * 16 + q) * 132 + sj; const float a = AA[o]; hcur = a * hcur + BB[o]; acum *= a; BB[o] = hcur; AA[o] = acum; }
;             __syncthreads();
;             const unsigned gw[8] = {gc0.x, gc0.y, gc0.z, gc0.w, gc1.x, gc1.y, gc1.z, gc1.w};
;             unsigned oy[8], ow[8];
; #pragma unroll
;             for (int q = 0; q < 8; ++q) { const float g0 = gelu_tanh(bflo(gw[q])), g1 = gelu_tanh(bfhi(gw[q]));
;                 oy[q] = pk2(BB[m * 132 + j0 + 2 * q] * g0, BB[m * 132 + j0 + 2 * q + 1] * g1);
;                 ow[q] = pk2(AA[m * 132 + j0 + 2 * q] * g0, AA[m * 132 + j0 + 2 * q + 1] * g1); }
.LBB0_269:
	s_or_b64 exec, exec, s[6:7]
	v_fma_f32 v238, v50, v222, v238
	v_fmac_f32_e32 v239, v238, v223
	v_mul_f32_e32 v222, v51, v222
	v_mul_f32_e32 v223, v222, v223
	ds_write2_b32 v158, v238, v239 offset1:132
	ds_write2_b32 v66, v222, v223 offset1:132
	v_fma_f32 v240, v239, v224, v240
	v_fmac_f32_e32 v241, v240, v225
	v_mul_f32_e32 v224, v223, v224
	v_mul_f32_e32 v225, v224, v225
	ds_write2_b32 v65, v240, v241 offset0:8 offset1:140
	ds_write2_b32 v64, v224, v225 offset0:8 offset1:140
	v_fma_f32 v244, v241, v226, v244
	v_fmac_f32_e32 v245, v244, v227
	v_mul_f32_e32 v226, v225, v226
	v_mul_f32_e32 v227, v226, v227
	ds_write2_b32 v63, v244, v245 offset0:16 offset1:148
	ds_write2_b32 v62, v226, v227 offset0:16 offset1:148
	v_fma_f32 v246, v245, v228, v246
	v_fmac_f32_e32 v247, v246, v229
	v_mul_f32_e32 v228, v227, v228
	v_mul_f32_e32 v229, v228, v229
	ds_write2_b32 v61, v246, v247 offset0:24 offset1:156
	ds_write2_b32 v60, v228, v229 offset0:24 offset1:156
	v_fma_f32 v248, v247, v230, v248
	v_fmac_f32_e32 v249, v248, v231
	v_mul_f32_e32 v230, v229, v230
	v_mul_f32_e32 v231, v230, v231
	ds_write2_b32 v59, v248, v249 offset0:32 offset1:164
	ds_write2_b32 v58, v230, v231 offset0:32 offset1:164
	v_fma_f32 v250, v249, v232, v250
	v_fmac_f32_e32 v251, v250, v233
	v_mul_f32_e32 v232, v231, v232
	v_mul_f32_e32 v233, v232, v233
	ds_write2_b32 v57, v250, v251 offset0:40 offset1:172
	ds_write2_b32 v56, v232, v233 offset0:40 offset1:172
	v_fma_f32 v252, v251, v234, v252
	v_fmac_f32_e32 v253, v252, v235
	v_mul_f32_e32 v234, v233, v234
	v_mul_f32_e32 v235, v234, v235
	ds_write2_b32 v55, v252, v253 offset0:48 offset1:180
	ds_write2_b32 v54, v234, v235 offset0:48 offset1:180
	v_fma_f32 v254, v253, v236, v254
	v_fmac_f32_e32 v255, v254, v237
	v_mul_f32_e32 v236, v235, v236
	v_mul_f32_e32 v237, v236, v237
	ds_write2_b32 v53, v254, v255 offset0:56 offset1:188
	ds_write2_b32 v52, v236, v237 offset0:56 offset1:188
	s_waitcnt lgkmcnt(0)
	s_barrier
	s_mov_b32 s100, 0xbdd2d3e7
	s_mov_b32 s101, 0xc0135761
	ds_read_b128 v[50:53], v164
	ds_read_b128 v[222:225], v164 offset:51200
	ds_read_b128 v[54:57], v164 offset:16
	ds_read_b128 v[226:229], v164 offset:51216
	ds_read_b128 v[58:61], v164 offset:32
	ds_read_b128 v[230:233], v164 offset:51232
	ds_read_b128 v[62:65], v164 offset:48
	ds_read_b128 v[234:237], v164 offset:51248
	v_lshlrev_b32_e32 v238, 16, v6
	v_lshlrev_b32_e32 v240, 16, v7
	v_and_b32_e32 v239, 0xffff0000, v6
	v_and_b32_e32 v241, 0xffff0000, v7
	v_pk_mul_f32 v[66:67], v[238:239], v[238:239]
	v_pk_mul_f32 v[68:69], v[240:241], v[240:241]
	v_pk_fma_f32 v[66:67], v[66:67], s[100:101], s[100:101] op_sel:[0,0,1] op_sel_hi:[1,0,1]
	v_pk_fma_f32 v[68:69], v[68:69], s[100:101], s[100:101] op_sel:[0,0,1] op_sel_hi:[1,0,1]
	v_pk_mul_f32 v[66:67], v[66:67], v[238:239]
	v_pk_mul_f32 v[68:69], v[68:69], v[240:241]
	v_exp_f32_e32 v66, v66
	v_exp_f32_e32 v67, v67
	v_exp_f32_e32 v68, v68
	v_exp_f32_e32 v69, v69
	v_pk_add_f32 v[66:67], v[66:67], 1.0 op_sel_hi:[1,0]
	v_pk_add_f32 v[68:69], v[68:69], 1.0 op_sel_hi:[1,0]
	v_rcp_f32_e32 v66, v66
	v_rcp_f32_e32 v67, v67
	v_rcp_f32_e32 v68, v68
	v_rcp_f32_e32 v69, v69
	v_pk_mul_f32 v[238:239], v[66:67], v[238:239]
	v_pk_mul_f32 v[240:241], v[68:69], v[240:241]
	v_lshlrev_b32_e32 v244, 16, v8
	v_lshlrev_b32_e32 v246, 16, v9
	v_and_b32_e32 v245, 0xffff0000, v8
	v_and_b32_e32 v247, 0xffff0000, v9
	v_pk_mul_f32 v[66:67], v[244:245], v[244:245]
	v_pk_mul_f32 v[68:69], v[246:247], v[246:247]
	v_pk_fma_f32 v[66:67], v[66:67], s[100:101], s[100:101] op_sel:[0,0,1] op_sel_hi:[1,0,1]
	v_pk_fma_f32 v[68:69], v[68:69], s[100:101], s[100:101] op_sel:[0,0,1] op_sel_hi:[1,0,1]
	v_pk_mul_f32 v[66:67], v[66:67], v[244:245]
	v_pk_mul_f32 v[68:69], v[68:69], v[246:247]
	v_exp_f32_e32 v66, v66
	v_exp_f32_e32 v67, v67
	v_exp_f32_e32 v68, v68
	v_exp_f32_e32 v69, v69
	v_pk_add_f32 v[66:67], v[66:67], 1.0 op_sel_hi:[1,0]
	v_pk_add_f32 v[68:69], v[68:69], 1.0 op_sel_hi:[1,0]
	v_rcp_f32_e32 v66, v66
	v_rcp_f32_e32 v67, v67
	v_rcp_f32_e32 v68, v68
	v_rcp_f32_e32 v69, v69
	v_pk_mul_f32 v[244:245], v[66:67], v[244:245]
	v_pk_mul_f32 v[246:247], v[68:69], v[246:247]
	v_lshlrev_b32_e32 v248, 16, v2
	v_lshlrev_b32_e32 v250, 16, v3
	v_and_b32_e32 v249, 0xffff0000, v2
	v_and_b32_e32 v251, 0xffff0000, v3
	v_pk_mul_f32 v[66:67], v[248:249], v[248:249]
	v_pk_mul_f32 v[68:69], v[250:251], v[250:251]
	v_pk_fma_f32 v[66:67], v[66:67], s[100:101], s[100:101] op_sel:[0,0,1] op_sel_hi:[1,0,1]
	v_pk_fma_f32 v[68:69], v[68:69], s[100:101], s[100:101] op_sel:[0,0,1] op_sel_hi:[1,0,1]
	v_pk_mul_f32 v[66:67], v[66:67], v[248:249]
	v_pk_mul_f32 v[68:69], v[68:69], v[250:251]
	v_exp_f32_e32 v66, v66
	v_exp_f32_e32 v67, v67
	v_exp_f32_e32 v68, v68
	v_exp_f32_e32 v69, v69
	v_pk_add_f32 v[66:67], v[66:67], 1.0 op_sel_hi:[1,0]
	v_pk_add_f32 v[68:69], v[68:69], 1.0 op_sel_hi:[1,0]
	v_rcp_f32_e32 v66, v66
	v_rcp_f32_e32 v67, v67
	v_rcp_f32_e32 v68, v68
	v_rcp_f32_e32 v69, v69
	v_pk_mul_f32 v[248:249], v[66:67], v[248:249]
	v_pk_mul_f32 v[250:251], v[68:69], v[250:251]
	v_lshlrev_b32_e32 v252, 16, v4
	v_lshlrev_b32_e32 v254, 16, v5
	v_and_b32_e32 v253, 0xffff0000, v4
	v_and_b32_e32 v255, 0xffff0000, v5
	v_pk_mul_f32 v[66:67], v[252:253], v[252:253]
	v_pk_mul_f32 v[68:69], v[254:255], v[254:255]
	v_pk_fma_f32 v[66:67], v[66:67], s[100:101], s[100:101] op_sel:[0,0,1] op_sel_hi:[1,0,1]
	v_pk_fma_f32 v[68:69], v[68:69], s[100:101], s[100:101] op_sel:[0,0,1] op_sel_hi:[1,0,1]
	v_pk_mul_f32 v[66:67], v[66:67], v[252:253]
	v_pk_mul_f32 v[68:69], v[68:69], v[254:255]
	v_exp_f32_e32 v66, v66
	v_exp_f32_e32 v67, v67
	v_exp_f32_e32 v68, v68
	v_exp_f32_e32 v69, v69
	v_pk_add_f32 v[66:67], v[66:67], 1.0 op_sel_hi:[1,0]
	v_pk_add_f32 v[68:69], v[68:69], 1.0 op_sel_hi:[1,0]
	v_rcp_f32_e32 v66, v66
	v_rcp_f32_e32 v67, v67
	v_rcp_f32_e32 v68, v68
	v_rcp_f32_e32 v69, v69
	v_pk_mul_f32 v[252:253], v[66:67], v[252:253]
	v_pk_mul_f32 v[254:255], v[68:69], v[254:255]
	s_waitcnt lgkmcnt(0)
; __device__ __forceinline__ unsigned pk2(float lo, float hi) { const f32x2c_t v = {lo, hi}; const bf16x2c_t b = __builtin_convertvector(v, bf16x2c_t); return __builtin_bit_cast(unsigned, b); }
; __device__ __forceinline__ float bflo(unsigned w) { return __uint_as_float(w << 16); }
; __device__ __forceinline__ float bfhi(unsigned w) { return __uint_as_float(w & 0xffff0000u); }
; __device__ __forceinline__ float gelu_tanh(float x) { const float y = 0.7978845608028654f * (x + 0.044715f * x * x * x); return x * __builtin_amdgcn_rcpf(1.0f + fexp_(-2.0f * y)); }
; template <int ISV>
; __device__ __forceinline__ void quant_finish(const QRow& q, unsigned char* qtab, float* scales, int e, int lane) {
;     float amax = 0.f;
; #pragma unroll
;     for (int j = 0; j < 8; ++j) amax = fmaxf(amax, fmaxf(fmaxf(fabsf(q.v[j].x), fabsf(q.v[j].y)), fmaxf(fabsf(q.v[j].z), fabsf(q.v[j].w))));
;     amax = wave_max(amax);
;     unsigned* qp = (unsigned*)qtab + (size_t)e * 64;
;     {
;         const float inv = amax > 0.f ? 127.0f / amax : 0.f;
;         if (lane == 0) scales[e] = amax * (1.0f / 127.0f);
; template <int MODE> ...
;     ...
;             const unsigned gw[8] = {gc0.x, gc0.y, gc0.z, gc0.w, gc1.x, gc1.y, gc1.z, gc1.w};
;             unsigned oy[8], ow[8];
; #pragma unroll
;             for (int q = 0; q < 8; ++q) { const float g0 = gelu_tanh(bflo(gw[q])), g1 = gelu_tanh(bfhi(gw[q]));
;                 oy[q] = pk2(BB[m * 132 + j0 + 2 * q] * g0, BB[m * 132 + j0 + 2 * q + 1] * g1);
;                 ow[q] = pk2(AA[m * 132 + j0 + 2 * q] * g0, AA[m * 132 + j0 + 2 * q + 1] * g1); }
;             const size_t yo = (size_t)(n * 64 + m) * 1024 + c0 + j0;
;             *(u32x4*)(Y0 + yo) = (u32x4){oy[0], oy[1], oy[2], oy[3]}; *(u32x4*)(Y0 + yo + 8) = (u32x4){oy[4], oy[5], oy[6], oy[7]};
;             *(u32x4*)(W0 + yo) = (u32x4){ow[0], ow[1], ow[2], ow[3]}; *(u32x4*)(W0 + yo + 8) = (u32x4){ow[4], ow[5], ow[6], ow[7]};
	v_pk_mul_f32 v[66:67], v[238:239], v[50:51]
	v_pk_mul_f32 v[238:239], v[238:239], v[222:223]
	v_cvt_pk_bf16_f32 v50, v66, v67
	v_cvt_pk_bf16_f32 v6, v238, v239
	v_pk_mul_f32 v[68:69], v[240:241], v[52:53]
	v_pk_mul_f32 v[240:241], v[240:241], v[224:225]
	v_cvt_pk_bf16_f32 v51, v68, v69
	v_cvt_pk_bf16_f32 v7, v240, v241
	v_pk_mul_f32 v[66:67], v[244:245], v[54:55]
	v_pk_mul_f32 v[244:245], v[244:245], v[226:227]
	v_cvt_pk_bf16_f32 v52, v66, v67
	v_cvt_pk_bf16_f32 v8, v244, v245
	v_pk_mul_f32 v[68:69], v[246:247], v[56:57]
	v_pk_mul_f32 v[246:247], v[246:247], v[228:229]
	v_cvt_pk_bf16_f32 v53, v68, v69
	v_cvt_pk_bf16_f32 v9, v246, v247
	v_pk_mul_f32 v[66:67], v[248:249], v[58:59]
	v_pk_mul_f32 v[248:249], v[248:249], v[230:231]
	v_cvt_pk_bf16_f32 v54, v66, v67
	v_cvt_pk_bf16_f32 v2, v248, v249
	v_pk_mul_f32 v[68:69], v[250:251], v[60:61]
	v_pk_mul_f32 v[250:251], v[250:251], v[232:233]
	v_cvt_pk_bf16_f32 v55, v68, v69
	v_cvt_pk_bf16_f32 v3, v250, v251
	v_pk_mul_f32 v[66:67], v[252:253], v[62:63]
	v_pk_mul_f32 v[252:253], v[252:253], v[234:235]
	v_cvt_pk_bf16_f32 v56, v66, v67
	v_cvt_pk_bf16_f32 v4, v252, v253
	v_pk_mul_f32 v[68:69], v[254:255], v[64:65]
	v_pk_mul_f32 v[254:255], v[254:255], v[236:237]
	v_cvt_pk_bf16_f32 v57, v68, v69
	v_cvt_pk_bf16_f32 v5, v254, v255
	v_lshl_add_u32 v58, s0, 6, v79
	v_ashrrev_i32_e32 v59, 31, v58
	v_lshlrev_b64 v[58:59], 10, v[58:59]
	v_or_b32_e32 v58, s18, v58
	v_or_b32_e32 v58, v58, v78
	v_lshlrev_b64 v[58:59], 1, v[58:59]
	v_lshl_add_u64 v[60:61], s[72:73], 0, v[58:59]
	v_lshl_add_u64 v[62:63], s[90:91], 0, v[58:59]
	global_store_dwordx4 v[60:61], v[50:53], off
	global_store_dwordx4 v[60:61], v[54:57], off offset:16
	global_store_dwordx4 v[62:63], v[6:9], off
	global_store_dwordx4 v[62:63], v[2:5], off offset:16
	s_waitcnt vmcnt(11)
	s_nop 0
	v_max_f32_e64 v2, |v49|, |v49|
	v_max_f32_e64 v3, |v48|, |v48|
	v_max_f32_e32 v2, v3, v2
	s_waitcnt vmcnt(10)
	v_max_f32_e64 v3, |v45|, |v45|
	v_max_f32_e64 v4, |v44|, |v44|
	v_max_f32_e32 v3, v4, v3
	v_max3_f32 v2, |v46|, |v47|, v2
	v_max3_f32 v3, |v42|, |v43|, v3
	v_max3_f32 v2, v2, 0, v3
	s_waitcnt vmcnt(9)
	v_max_f32_e64 v3, |v41|, |v41|
	v_max_f32_e64 v4, |v40|, |v40|
	v_max_f32_e32 v3, v4, v3
	s_waitcnt vmcnt(8)
	v_max_f32_e64 v4, |v37|, |v37|
	v_max_f32_e64 v5, |v36|, |v36|
	v_max_f32_e32 v4, v5, v4
	v_max3_f32 v3, |v38|, |v39|, v3
	v_max3_f32 v4, |v34|, |v35|, v4
	v_max3_f32 v2, v2, v3, v4
	s_waitcnt vmcnt(7)
	v_max_f32_e64 v3, |v33|, |v33|
	v_max_f32_e64 v4, |v32|, |v32|
	v_max_f32_e32 v3, v4, v3
	s_waitcnt vmcnt(6)
	v_max_f32_e64 v4, |v29|, |v29|
	v_max_f32_e64 v5, |v28|, |v28|
	v_max_f32_e32 v4, v5, v4
	v_max3_f32 v3, |v30|, |v31|, v3
	v_max3_f32 v4, |v26|, |v27|, v4
	v_max3_f32 v2, v2, v3, v4
	s_waitcnt vmcnt(5)
	v_max_f32_e64 v3, |v25|, |v25|
	v_max_f32_e64 v4, |v24|, |v24|
	v_max_f32_e32 v3, v4, v3
	s_waitcnt vmcnt(4)
	v_max_f32_e64 v4, |v21|, |v21|
	v_max_f32_e64 v5, |v20|, |v20|
	v_max_f32_e32 v4, v5, v4
	v_max3_f32 v3, |v22|, |v23|, v3
	v_max3_f32 v4, |v18|, |v19|, v4
	v_max3_f32 v2, v2, v3, v4
	ds_bpermute_b32 v3, v114, v2
	s_waitcnt lgkmcnt(0)
	v_max_f32_e32 v3, v3, v3
	v_max_f32_e32 v2, v2, v3
	ds_bpermute_b32 v3, v115, v2
	s_waitcnt lgkmcnt(0)
	v_max_f32_e32 v3, v3, v3
	v_max_f32_e32 v2, v2, v3
	ds_bpermute_b32 v3, v116, v2
	s_waitcnt lgkmcnt(0)
	v_max_f32_e32 v3, v3, v3
	v_max_f32_e32 v2, v2, v3
	ds_bpermute_b32 v3, v117, v2
	s_waitcnt lgkmcnt(0)
	v_max_f32_e32 v3, v3, v3
	v_max_f32_e32 v2, v2, v3
	ds_bpermute_b32 v3, v118, v2
	s_waitcnt lgkmcnt(0)
	v_max_f32_e32 v3, v3, v3
	v_max_f32_e32 v2, v2, v3
	ds_bpermute_b32 v3, v119, v2
	s_waitcnt lgkmcnt(0)
	v_max_f32_e32 v3, v3, v3
	v_max_f32_e32 v2, v2, v3
	s_and_saveexec_b64 s[6:7], s[40:41]
	s_cbranch_execz .LBB0_240
	s_lshl_b64 s[22:23], s[48:49], 2
	s_add_u32 s22, s86, s22
	s_addc_u32 s23, s87, s23
	v_mul_f32_e32 v3, 0x3c010204, v2
	global_store_dword v85, v3, s[22:23]
	s_branch .LBB0_240
